# 16 conversion sub-queues instead of 8
# speedup vs baseline: 1.0054x; 1.0000x over previous
; #define LAS __attribute__((address_space(3)))
; DI kptr_t kargs_now() { kptr_t p = (kptr_t)__builtin_amdgcn_kernarg_segment_ptr(); asm volatile("" : "+s"(p)); return p; }
; #define RI_NEXT(D_) do { if (q.cnt == 8) { int b_ = 0; if (F.lane == 0) b_ = (int)__hip_atomic_fetch_add(qctr, 8u, __ATOMIC_RELAXED, __HIP_MEMORY_SCOPE_AGENT); q.base = __builtin_amdgcn_readfirstlane(b_); q.cnt = 0; } \
;         D_ = decode_item(KA, F.ws, kind, q.base + q.cnt); ++q.cnt; } while (0)
; DI void run_items1(Frame& F, int kind, int quota, QState& q) {
;     const kptr_t KA = kargs_now();
;     LAS float* scr = (LAS float*)(F.lds + F.wave * 16384);
;     unsigned* qctr = F.ctl + CW_QUEUE + 64 * kind;
;     ...
;     if (quota == 0) return;
;     TItem d; RI_NEXT(d); if (!d.valid) return;
; DI void phase_attn(Frame& F, int l) {
;     ...
;     QState cq; cq.base = 0; cq.cnt = 8;
;     constexpr int SLOT_ITEMS = 3;
;     if (F.bid & 1) { __syncthreads(); run_items1(F, 1 + l, SLOT_ITEMS, cq); }
.LBB0_398:
	v_readlane_b32 s8, v255, 14
	v_readlane_b32 s4, v253, 8
	s_lshl_b32 s58, s8, 6
	v_readlane_b32 s6, v253, 10
	v_readlane_b32 s7, v253, 11
	s_lshl_b64 s[0:1], s[58:59], 2
	s_mov_b64 s[2:3], s[6:7]
	s_add_u32 s0, s2, s0
	s_addc_u32 s1, s3, s1
	v_readlane_b32 s9, v255, 15
	s_add_u32 s12, s0, 0x8100
	s_addc_u32 s13, s1, 0
	v_readlane_b32 s100, v253, 29
	s_lshr_b32 s100, s100, 1
	s_and_b32 s100, s100, 15
	s_lshl_b32 s0, s100, 8
	s_mul_i32 s1, s8, 0xf00
	s_add_i32 s0, s0, s1
	s_add_i32 s0, s0, 0x1300
	s_add_u32 s12, s12, s0
	s_addc_u32 s13, s13, 0
	s_lshl_b64 s[0:1], s[8:9], 25
	v_writelane_b32 v255, s0, 16
	s_lshl_b64 s[62:63], s[8:9], 5
	s_lshl_b32 s2, s8, 20
	v_writelane_b32 v255, s1, 17
	s_mov_b32 s3, s59
	v_readlane_b32 s0, v253, 33
	v_writelane_b32 v255, s2, 18
	s_add_u32 s76, s0, s2
	v_readlane_b32 s0, v253, 34
	v_writelane_b32 v255, s3, 19
	s_addc_u32 s77, s0, 0
	s_lshl_b64 s[20:21], s[8:9], 21
	s_lshl_b64 s[0:1], s[8:9], 20
	v_readlane_b32 s2, v253, 35
	s_add_u32 s22, s2, s0
	v_readlane_b32 s2, v253, 36
	s_addc_u32 s23, s2, s1
	v_readlane_b32 s2, v253, 37
	s_add_u32 s24, s2, s0
	v_readlane_b32 s0, v253, 38
	s_addc_u32 s25, s0, s1
	s_lshl_b64 s[26:27], s[8:9], 24
	v_readlane_b32 s0, v253, 39
	s_add_u32 s14, s0, s44
	v_readlane_b32 s0, v253, 40
	s_addc_u32 s15, s0, s45
	s_mov_b32 s0, -1
	s_mov_b32 s95, 0
	v_mbcnt_lo_u32_b32 v0, s0, 0
	v_mbcnt_hi_u32_b32 v186, s0, v0
	v_readlane_b32 s0, v253, 29
	s_mov_b32 s51, s0
	s_mov_b64 s[30:31], s[70:71]
	s_bitcmp0_b32 s51, 0
	s_mov_b32 s63, 4
	v_readlane_b32 s5, v253, 9
	v_readlane_b32 s1, v253, 30
	s_cbranch_scc1 .LBB0_472
	s_mov_b64 s[6:7], s[70:71]
	v_mov_b32_e32 v0, 0
	v_cmp_eq_u32_e64 s[4:5], 0, v186
	s_waitcnt vmcnt(63) expcnt(7) lgkmcnt(15)
	s_barrier
	s_and_saveexec_b64 s[2:3], s[4:5]
	s_cbranch_execz .LBB0_403
	s_mov_b64 s[10:11], exec
	v_mbcnt_lo_u32_b32 v0, s10, 0
	v_mbcnt_hi_u32_b32 v0, s11, v0
	v_cmp_eq_u32_e32 vcc, 0, v0
	s_and_saveexec_b64 s[8:9], vcc
	s_cbranch_execz .LBB0_402
	s_bcnt1_i32_b64 s0, s[10:11]
	s_lshl_b32 s0, s0, 2
	v_mov_b32_e32 v2, s0
	global_atomic_add v2, v1, v2, s[12:13] sc0

; DI const float* inp(kptr_t k, int i) { return (const float*)k[i]; }
; DI int imap(int n, int H) { return ((n % H) / 128) * 256 + (n / H) * 128 + (n % 128); }
; DI TItem decode_item(kptr_t KA, unsigned char* ws, int kind, int it) {
;     TItem d; d.valid = it < (kind == 0 ? DEPTH * IT_SMALL : IT_EXP); if (!d.valid) it = 0;
;     const int l = kind == 0 ? it / IT_SMALL : kind - 1; int r = kind == 0 ? it % IT_SMALL : IT_SMALL + it;
;     const float* W; unsigned char* WT; int K, N, H = 0; bool f8 = false;
;     int nsub = 0, Kd = 0, kofs = 0;
;     if (r < IT_IN) { W = inp(KA, I_WIN) + (size_t)l * D * INW; K = D; N = INW;
;         WT = ws + WS_WIN + (size_t)l * INW * D; f8 = true; }
;     else if ((r -= IT_IN) < IT_GLU) { W = inp(KA, I_WGLU) + (size_t)l * SW * 1024; WT = ws + WS_WGLU + (size_t)l * 1024 * SW * 2; K = SW; N = 1024; H = 512; }
;     else if ((r -= IT_GLU) < IT_ATT) { W = inp(KA, I_WATTO) + (size_t)l * AW * D; WT = ws + WS_WCAT + (size_t)l * D * D; K = AW; N = D; Kd = D; f8 = true; }
;     else if ((r -= IT_ATT) < IT_SSMO) { W = inp(KA, I_WSSMO) + (size_t)l * SW * D; WT = ws + WS_WCAT + (size_t)l * D * D; K = SW; N = D; Kd = D; kofs = AW; f8 = true; }
;     else if ((r -= IT_SSMO) < IT_OUT) { W = inp(KA, I_WOUT) + (size_t)l * D * D; WT = ws + WS_WOUT + (size_t)l * D * D; K = D; N = D; f8 = true; }
;     else if ((r -= IT_OUT) < NE * IT_W1) { const int e = r / IT_W1; r %= IT_W1; W = inp(KA, I_WEXPIN) + ((size_t)l * NE + e) * D * 2048; WT = ws + WS_W1 + ((size_t)l * NE + e) * 2048 * D; K = D; N = 2048; H = 1024; f8 = true; }
;     else { r -= NE * IT_W1; const int e = r / IT_W2; r %= IT_W2; W = inp(KA, I_WEXPOUT) + ((size_t)l * NE + e) * DFF * D; WT = ws + WS_W2 + ((size_t)l * NE + e) * D * DFF; K = DFF; N = D; f8 = true; }
;     const int nblk = N / 64, kb = r / nblk, nb = r % nblk, n0 = nb * 64;
;     d.W = W; d.WT = WT; d.N = N; d.Kd = Kd ? Kd : K; d.kofs = kofs; d.drow0 = (H ? imap(n0, H) : n0) - nsub; d.k0 = kb * 64; d.n0 = n0; d.f8 = f8;
.LBB0_403:
	s_or_b64 exec, exec, s[2:3]
	v_readfirstlane_b32 s95, v0
	s_lshl_b32 s101, s95, 4
	s_or_b32 s101, s101, s100
	s_cmpk_lt_i32 s101, 0x6000
	s_cselect_b64 s[2:3], -1, 0
	s_and_b64 s[0:1], s[2:3], exec
	s_cselect_b32 s36, s101, 0
	s_add_i32 s0, s36, 0x680
	s_cmpk_gt_i32 s36, 0xfd7f
	s_mov_b64 s[18:19], -1
	s_cbranch_scc0 .LBB0_424
	s_mov_b64 s[34:35], -1
	s_cmpk_gt_u32 s0, 0x47f
	s_mov_b64 s[8:9], -1
	s_cbranch_scc0 .LBB0_421
	s_cmpk_gt_u32 s0, 0x4ff
	s_cbranch_scc0 .LBB0_418
	s_cmpk_gt_u32 s0, 0x57f
	s_cbranch_scc0 .LBB0_415
	s_cmp_lt_u32 s36, 0xfffff980
	s_cbranch_scc0 .LBB0_412
	s_mov_b64 s[28:29], -1
	s_cmpk_gt_u32 s0, 0x467f
	s_cbranch_scc0 .LBB0_410
	s_add_i32 s1, s36, 0xffffc000
	s_lshr_b32 s58, s1, 8
	s_load_dwordx2 s[8:9], s[6:7], 0xd0
	s_and_b32 s1, s36, 0xff
	s_lshl_b64 s[10:11], s[58:59], 20
	v_readlane_b32 s16, v255, 16
	v_readlane_b32 s17, v255, 17
	s_add_u32 s10, s10, s16
	s_addc_u32 s11, s11, s17
	s_lshl_b64 s[16:17], s[10:11], 2
	s_waitcnt lgkmcnt(0)
	s_add_u32 s16, s8, s16
	s_addc_u32 s17, s9, s17
	v_readlane_b32 s8, v253, 45
	s_add_u32 s10, s8, s10
	v_readlane_b32 s8, v253, 46
	s_addc_u32 s11, s8, s11
	s_mov_b64 s[8:9], 0

; DI const float* inp(kptr_t k, int i) { return (const float*)k[i]; }
; DI int imap(int n, int H) { return ((n % H) / 128) * 256 + (n / H) * 128 + (n % 128); }
; DI TItem decode_item(kptr_t KA, unsigned char* ws, int kind, int it) {
;     TItem d; d.valid = it < (kind == 0 ? DEPTH * IT_SMALL : IT_EXP); if (!d.valid) it = 0;
;     const int l = kind == 0 ? it / IT_SMALL : kind - 1; int r = kind == 0 ? it % IT_SMALL : IT_SMALL + it;
;     const float* W; unsigned char* WT; int K, N, H = 0; bool f8 = false;
;     int nsub = 0, Kd = 0, kofs = 0;
;     if (r < IT_IN) { W = inp(KA, I_WIN) + (size_t)l * D * INW; K = D; N = INW;
;         WT = ws + WS_WIN + (size_t)l * INW * D; f8 = true; }
;     else if ((r -= IT_IN) < IT_GLU) { W = inp(KA, I_WGLU) + (size_t)l * SW * 1024; WT = ws + WS_WGLU + (size_t)l * 1024 * SW * 2; K = SW; N = 1024; H = 512; }
;     else if ((r -= IT_GLU) < IT_ATT) { W = inp(KA, I_WATTO) + (size_t)l * AW * D; WT = ws + WS_WCAT + (size_t)l * D * D; K = AW; N = D; Kd = D; f8 = true; }
;     else if ((r -= IT_ATT) < IT_SSMO) { W = inp(KA, I_WSSMO) + (size_t)l * SW * D; WT = ws + WS_WCAT + (size_t)l * D * D; K = SW; N = D; Kd = D; kofs = AW; f8 = true; }
;     else if ((r -= IT_SSMO) < IT_OUT) { W = inp(KA, I_WOUT) + (size_t)l * D * D; WT = ws + WS_WOUT + (size_t)l * D * D; K = D; N = D; f8 = true; }
;     else if ((r -= IT_OUT) < NE * IT_W1) { const int e = r / IT_W1; r %= IT_W1; W = inp(KA, I_WEXPIN) + ((size_t)l * NE + e) * D * 2048; WT = ws + WS_W1 + ((size_t)l * NE + e) * 2048 * D; K = D; N = 2048; H = 1024; f8 = true; }
;     else { r -= NE * IT_W1; const int e = r / IT_W2; r %= IT_W2; W = inp(KA, I_WEXPOUT) + ((size_t)l * NE + e) * DFF * D; WT = ws + WS_W2 + ((size_t)l * NE + e) * D * DFF; K = DFF; N = D; f8 = true; }
;     const int nblk = N / 64, kb = r / nblk, nb = r % nblk, n0 = nb * 64;
;     d.W = W; d.WT = WT; d.N = N; d.Kd = Kd ? Kd : K; d.kofs = kofs; d.drow0 = (H ? imap(n0, H) : n0) - nsub; d.k0 = kb * 64; d.n0 = n0; d.f8 = f8;
.LBB0_437:
	s_add_i32 s9, s63, s95
	s_lshl_b32 s9, s9, 4
	s_or_b32 s9, s9, s100
	s_cmpk_lt_i32 s9, 0x6000
	s_cselect_b64 s[2:3], -1, 0
	s_and_b64 s[0:1], s[2:3], exec
	s_cselect_b32 s9, s9, 0
	s_add_i32 s0, s9, 0x680
	s_cmpk_gt_i32 s9, 0xfd7f
	s_mov_b64 s[18:19], -1
	s_cbranch_scc0 .LBB0_458
	s_mov_b64 s[16:17], -1
	s_cmpk_gt_u32 s0, 0x47f
	s_cbranch_scc0 .LBB0_455
	s_cmpk_gt_u32 s0, 0x4ff
	s_cbranch_scc0 .LBB0_452
	s_cmpk_gt_u32 s0, 0x57f
	s_cbranch_scc0 .LBB0_449
	s_cmp_lt_u32 s9, 0xfffff980
	s_cbranch_scc0 .LBB0_446
	s_mov_b64 s[56:57], -1
	s_cmpk_gt_u32 s0, 0x467f
	s_cbranch_scc0 .LBB0_444
	s_add_i32 s1, s9, 0xffffc000
	s_lshr_b32 s58, s1, 8
	s_load_dwordx2 s[18:19], s[6:7], 0xd0
	s_and_b32 s1, s9, 0xff
	s_lshl_b64 s[28:29], s[58:59], 20
	v_readlane_b32 s36, v255, 16
	v_readlane_b32 s37, v255, 17
	s_add_u32 s28, s28, s36
	s_addc_u32 s29, s29, s37
	s_lshl_b64 s[36:37], s[28:29], 2
	s_waitcnt lgkmcnt(0)
	s_add_u32 s42, s18, s36
	s_addc_u32 s43, s19, s37
	v_readlane_b32 s18, v253, 45
	s_add_u32 s28, s18, s28
	v_readlane_b32 s18, v253, 46
	s_addc_u32 s29, s18, s29
	s_mov_b64 s[18:19], 0

; DI const float* inp(kptr_t k, int i) { return (const float*)k[i]; }
; DI int imap(int n, int H) { return ((n % H) / 128) * 256 + (n / H) * 128 + (n % 128); }
; DI TItem decode_item(kptr_t KA, unsigned char* ws, int kind, int it) {
;     TItem d; d.valid = it < (kind == 0 ? DEPTH * IT_SMALL : IT_EXP); if (!d.valid) it = 0;
;     const int l = kind == 0 ? it / IT_SMALL : kind - 1; int r = kind == 0 ? it % IT_SMALL : IT_SMALL + it;
;     const float* W; unsigned char* WT; int K, N, H = 0; bool f8 = false;
;     int nsub = 0, Kd = 0, kofs = 0;
;     if (r < IT_IN) { W = inp(KA, I_WIN) + (size_t)l * D * INW; K = D; N = INW;
;         WT = ws + WS_WIN + (size_t)l * INW * D; f8 = true; }
;     else if ((r -= IT_IN) < IT_GLU) { W = inp(KA, I_WGLU) + (size_t)l * SW * 1024; WT = ws + WS_WGLU + (size_t)l * 1024 * SW * 2; K = SW; N = 1024; H = 512; }
;     else if ((r -= IT_GLU) < IT_ATT) { W = inp(KA, I_WATTO) + (size_t)l * AW * D; WT = ws + WS_WCAT + (size_t)l * D * D; K = AW; N = D; Kd = D; f8 = true; }
;     else if ((r -= IT_ATT) < IT_SSMO) { W = inp(KA, I_WSSMO) + (size_t)l * SW * D; WT = ws + WS_WCAT + (size_t)l * D * D; K = SW; N = D; Kd = D; kofs = AW; f8 = true; }
;     else if ((r -= IT_SSMO) < IT_OUT) { W = inp(KA, I_WOUT) + (size_t)l * D * D; WT = ws + WS_WOUT + (size_t)l * D * D; K = D; N = D; f8 = true; }
;     else if ((r -= IT_OUT) < NE * IT_W1) { const int e = r / IT_W1; r %= IT_W1; W = inp(KA, I_WEXPIN) + ((size_t)l * NE + e) * D * 2048; WT = ws + WS_W1 + ((size_t)l * NE + e) * 2048 * D; K = D; N = 2048; H = 1024; f8 = true; }
;     else { r -= NE * IT_W1; const int e = r / IT_W2; r %= IT_W2; W = inp(KA, I_WEXPOUT) + ((size_t)l * NE + e) * DFF * D; WT = ws + WS_W2 + ((size_t)l * NE + e) * D * DFF; K = DFF; N = D; f8 = true; }
;     const int nblk = N / 64, kb = r / nblk, nb = r % nblk, n0 = nb * 64;
;     d.W = W; d.WT = WT; d.N = N; d.Kd = Kd ? Kd : K; d.kofs = kofs; d.drow0 = (H ? imap(n0, H) : n0) - nsub; d.k0 = kb * 64; d.n0 = n0; d.f8 = f8;
.LBB0_575:
	s_add_i32 s8, s63, s95
	s_lshl_b32 s8, s8, 4
	s_or_b32 s8, s8, s100
	s_cmpk_lt_i32 s8, 0x6000
	s_cselect_b64 s[2:3], -1, 0
	s_and_b64 s[0:1], s[2:3], exec
	s_cselect_b32 s36, s8, 0
	s_add_i32 s0, s36, 0x680
	s_cmpk_gt_i32 s36, 0xfd7f
	s_mov_b64 s[18:19], -1
	s_cbranch_scc0 .LBB0_596
	s_mov_b64 s[42:43], -1
	s_cmpk_gt_u32 s0, 0x47f
	s_mov_b64 s[8:9], -1
	s_cbranch_scc0 .LBB0_593
	s_cmpk_gt_u32 s0, 0x4ff
	s_cbranch_scc0 .LBB0_590
	s_cmpk_gt_u32 s0, 0x57f
	s_cbranch_scc0 .LBB0_587
	s_cmp_lt_u32 s36, 0xfffff980
	s_cbranch_scc0 .LBB0_584
	s_mov_b64 s[28:29], -1
	s_cmpk_gt_u32 s0, 0x467f
	s_cbranch_scc0 .LBB0_582
	s_add_i32 s1, s36, 0xffffc000
	s_lshr_b32 s58, s1, 8
	s_load_dwordx2 s[8:9], s[6:7], 0xd0
	s_and_b32 s1, s36, 0xff
	s_lshl_b64 s[10:11], s[58:59], 20
	v_readlane_b32 s16, v255, 16
	v_readlane_b32 s17, v255, 17
	s_add_u32 s10, s10, s16
	s_addc_u32 s11, s11, s17
	s_lshl_b64 s[16:17], s[10:11], 2
	s_waitcnt lgkmcnt(0)
	s_add_u32 s16, s8, s16
	s_addc_u32 s17, s9, s17
	v_readlane_b32 s8, v253, 45
	s_add_u32 s10, s8, s10
	v_readlane_b32 s8, v253, 46
	s_addc_u32 s11, s8, s11
	s_mov_b64 s[8:9], 0

; DI const float* inp(kptr_t k, int i) { return (const float*)k[i]; }
; DI int imap(int n, int H) { return ((n % H) / 128) * 256 + (n / H) * 128 + (n % 128); }
; DI TItem decode_item(kptr_t KA, unsigned char* ws, int kind, int it) {
;     TItem d; d.valid = it < (kind == 0 ? DEPTH * IT_SMALL : IT_EXP); if (!d.valid) it = 0;
;     const int l = kind == 0 ? it / IT_SMALL : kind - 1; int r = kind == 0 ? it % IT_SMALL : IT_SMALL + it;
;     const float* W; unsigned char* WT; int K, N, H = 0; bool f8 = false;
;     int nsub = 0, Kd = 0, kofs = 0;
;     if (r < IT_IN) { W = inp(KA, I_WIN) + (size_t)l * D * INW; K = D; N = INW;
;         WT = ws + WS_WIN + (size_t)l * INW * D; f8 = true; }
;     else if ((r -= IT_IN) < IT_GLU) { W = inp(KA, I_WGLU) + (size_t)l * SW * 1024; WT = ws + WS_WGLU + (size_t)l * 1024 * SW * 2; K = SW; N = 1024; H = 512; }
;     else if ((r -= IT_GLU) < IT_ATT) { W = inp(KA, I_WATTO) + (size_t)l * AW * D; WT = ws + WS_WCAT + (size_t)l * D * D; K = AW; N = D; Kd = D; f8 = true; }
;     else if ((r -= IT_ATT) < IT_SSMO) { W = inp(KA, I_WSSMO) + (size_t)l * SW * D; WT = ws + WS_WCAT + (size_t)l * D * D; K = SW; N = D; Kd = D; kofs = AW; f8 = true; }
;     else if ((r -= IT_SSMO) < IT_OUT) { W = inp(KA, I_WOUT) + (size_t)l * D * D; WT = ws + WS_WOUT + (size_t)l * D * D; K = D; N = D; f8 = true; }
;     else if ((r -= IT_OUT) < NE * IT_W1) { const int e = r / IT_W1; r %= IT_W1; W = inp(KA, I_WEXPIN) + ((size_t)l * NE + e) * D * 2048; WT = ws + WS_W1 + ((size_t)l * NE + e) * 2048 * D; K = D; N = 2048; H = 1024; f8 = true; }
;     else { r -= NE * IT_W1; const int e = r / IT_W2; r %= IT_W2; W = inp(KA, I_WEXPOUT) + ((size_t)l * NE + e) * DFF * D; WT = ws + WS_W2 + ((size_t)l * NE + e) * D * DFF; K = DFF; N = D; f8 = true; }
;     const int nblk = N / 64, kb = r / nblk, nb = r % nblk, n0 = nb * 64;
;     d.W = W; d.WT = WT; d.N = N; d.Kd = Kd ? Kd : K; d.kofs = kofs; d.drow0 = (H ? imap(n0, H) : n0) - nsub; d.k0 = kb * 64; d.n0 = n0; d.f8 = f8;
.LBB0_609:
	s_add_i32 s9, s63, s95
	s_lshl_b32 s9, s9, 4
	s_or_b32 s9, s9, s100
	s_cmpk_lt_i32 s9, 0x6000
	s_cselect_b64 s[2:3], -1, 0
	s_and_b64 s[0:1], s[2:3], exec
	s_cselect_b32 s9, s9, 0
	s_add_i32 s0, s9, 0x680
	s_cmpk_gt_i32 s9, 0xfd7f
	s_mov_b64 s[18:19], -1
	s_cbranch_scc0 .LBB0_630
	s_mov_b64 s[16:17], -1
	s_cmpk_gt_u32 s0, 0x47f
	s_cbranch_scc0 .LBB0_627
	s_cmpk_gt_u32 s0, 0x4ff
	s_cbranch_scc0 .LBB0_624
	s_cmpk_gt_u32 s0, 0x57f
	s_cbranch_scc0 .LBB0_621
	s_cmp_lt_u32 s9, 0xfffff980
	s_cbranch_scc0 .LBB0_618
	s_mov_b64 s[78:79], -1
	s_cmpk_gt_u32 s0, 0x467f
	s_cbranch_scc0 .LBB0_616
	s_add_i32 s1, s9, 0xffffc000
	s_lshr_b32 s58, s1, 8
	s_load_dwordx2 s[18:19], s[6:7], 0xd0
	s_and_b32 s1, s9, 0xff
	s_lshl_b64 s[28:29], s[58:59], 20
	v_readlane_b32 s36, v255, 16
	v_readlane_b32 s37, v255, 17
	s_add_u32 s28, s28, s36
	s_addc_u32 s29, s29, s37
	s_lshl_b64 s[36:37], s[28:29], 2
	s_waitcnt lgkmcnt(0)
	s_add_u32 s56, s18, s36
	s_addc_u32 s57, s19, s37
	v_readlane_b32 s18, v253, 45
	s_add_u32 s28, s18, s28
	v_readlane_b32 s18, v253, 46
	s_addc_u32 s29, s18, s29
	s_mov_b64 s[18:19], 0

; DI const float* inp(kptr_t k, int i) { return (const float*)k[i]; }
; DI int imap(int n, int H) { return ((n % H) / 128) * 256 + (n / H) * 128 + (n % 128); }
; DI TItem decode_item(kptr_t KA, unsigned char* ws, int kind, int it) {
;     TItem d; d.valid = it < (kind == 0 ? DEPTH * IT_SMALL : IT_EXP); if (!d.valid) it = 0;
;     const int l = kind == 0 ? it / IT_SMALL : kind - 1; int r = kind == 0 ? it % IT_SMALL : IT_SMALL + it;
;     const float* W; unsigned char* WT; int K, N, H = 0; bool f8 = false;
;     int nsub = 0, Kd = 0, kofs = 0;
;     if (r < IT_IN) { W = inp(KA, I_WIN) + (size_t)l * D * INW; K = D; N = INW;
;         WT = ws + WS_WIN + (size_t)l * INW * D; f8 = true; }
;     else if ((r -= IT_IN) < IT_GLU) { W = inp(KA, I_WGLU) + (size_t)l * SW * 1024; WT = ws + WS_WGLU + (size_t)l * 1024 * SW * 2; K = SW; N = 1024; H = 512; }
;     else if ((r -= IT_GLU) < IT_ATT) { W = inp(KA, I_WATTO) + (size_t)l * AW * D; WT = ws + WS_WCAT + (size_t)l * D * D; K = AW; N = D; Kd = D; f8 = true; }
;     else if ((r -= IT_ATT) < IT_SSMO) { W = inp(KA, I_WSSMO) + (size_t)l * SW * D; WT = ws + WS_WCAT + (size_t)l * D * D; K = SW; N = D; Kd = D; kofs = AW; f8 = true; }
;     else if ((r -= IT_SSMO) < IT_OUT) { W = inp(KA, I_WOUT) + (size_t)l * D * D; WT = ws + WS_WOUT + (size_t)l * D * D; K = D; N = D; f8 = true; }
;     else if ((r -= IT_OUT) < NE * IT_W1) { const int e = r / IT_W1; r %= IT_W1; W = inp(KA, I_WEXPIN) + ((size_t)l * NE + e) * D * 2048; WT = ws + WS_W1 + ((size_t)l * NE + e) * 2048 * D; K = D; N = 2048; H = 1024; f8 = true; }
;     else { r -= NE * IT_W1; const int e = r / IT_W2; r %= IT_W2; W = inp(KA, I_WEXPOUT) + ((size_t)l * NE + e) * DFF * D; WT = ws + WS_W2 + ((size_t)l * NE + e) * D * DFF; K = DFF; N = D; f8 = true; }
;     const int nblk = N / 64, kb = r / nblk, nb = r % nblk, n0 = nb * 64;
;     d.W = W; d.WT = WT; d.N = N; d.Kd = Kd ? Kd : K; d.kofs = kofs; d.drow0 = (H ? imap(n0, H) : n0) - nsub; d.k0 = kb * 64; d.n0 = n0; d.f8 = f8;
.LBB0_651:
	s_add_i32 s4, s63, s95
	s_lshl_b32 s4, s4, 4
	s_or_b32 s4, s4, s100
	s_cmpk_lt_i32 s4, 0x6000
	s_cselect_b64 s[2:3], -1, 0
	s_and_b64 s[0:1], s[2:3], exec
	s_cselect_b32 s33, s4, 0
	s_add_i32 s0, s33, 0x680
	s_cmpk_gt_i32 s33, 0xfd7f
	s_mov_b64 s[18:19], -1
	s_cbranch_scc0 .LBB0_671
	s_mov_b64 s[8:9], -1
	s_cmpk_gt_u32 s0, 0x47f
	s_cbranch_scc0 .LBB0_668
	s_cmpk_gt_u32 s0, 0x4ff
	s_mov_b64 s[34:35], -1
	s_cbranch_scc0 .LBB0_665
	s_cmpk_gt_u32 s0, 0x57f
	s_cbranch_scc0 .LBB0_663
	s_cmp_lt_u32 s33, 0xfffff980
	s_cbranch_scc0 .LBB0_660
	s_mov_b64 s[28:29], -1
	s_cmpk_gt_u32 s0, 0x467f
	s_mov_b64 s[16:17], -1
	s_cbranch_scc0 .LBB0_658
	s_add_i32 s1, s33, 0xffffc000
	s_lshr_b32 s58, s1, 8
	s_load_dwordx2 s[4:5], s[6:7], 0xd0
	s_and_b32 s1, s33, 0xff
	s_lshl_b64 s[10:11], s[58:59], 20
	v_readlane_b32 s16, v255, 16
	v_readlane_b32 s17, v255, 17
	s_add_u32 s10, s10, s16
	s_addc_u32 s11, s11, s17
	s_lshl_b64 s[16:17], s[10:11], 2
	s_waitcnt lgkmcnt(0)
	s_add_u32 s4, s4, s16
	s_addc_u32 s5, s5, s17
	v_readlane_b32 s16, v253, 45
	s_add_u32 s10, s16, s10
	v_readlane_b32 s16, v253, 46
	s_addc_u32 s11, s16, s11
	s_mov_b64 s[16:17], 0

; DI const float* inp(kptr_t k, int i) { return (const float*)k[i]; }
; DI int imap(int n, int H) { return ((n % H) / 128) * 256 + (n / H) * 128 + (n % 128); }
; DI TItem decode_item(kptr_t KA, unsigned char* ws, int kind, int it) {
;     TItem d; d.valid = it < (kind == 0 ? DEPTH * IT_SMALL : IT_EXP); if (!d.valid) it = 0;
;     const int l = kind == 0 ? it / IT_SMALL : kind - 1; int r = kind == 0 ? it % IT_SMALL : IT_SMALL + it;
;     const float* W; unsigned char* WT; int K, N, H = 0; bool f8 = false;
;     int nsub = 0, Kd = 0, kofs = 0;
;     if (r < IT_IN) { W = inp(KA, I_WIN) + (size_t)l * D * INW; K = D; N = INW;
;         WT = ws + WS_WIN + (size_t)l * INW * D; f8 = true; }
;     else if ((r -= IT_IN) < IT_GLU) { W = inp(KA, I_WGLU) + (size_t)l * SW * 1024; WT = ws + WS_WGLU + (size_t)l * 1024 * SW * 2; K = SW; N = 1024; H = 512; }
;     else if ((r -= IT_GLU) < IT_ATT) { W = inp(KA, I_WATTO) + (size_t)l * AW * D; WT = ws + WS_WCAT + (size_t)l * D * D; K = AW; N = D; Kd = D; f8 = true; }
;     else if ((r -= IT_ATT) < IT_SSMO) { W = inp(KA, I_WSSMO) + (size_t)l * SW * D; WT = ws + WS_WCAT + (size_t)l * D * D; K = SW; N = D; Kd = D; kofs = AW; f8 = true; }
;     else if ((r -= IT_SSMO) < IT_OUT) { W = inp(KA, I_WOUT) + (size_t)l * D * D; WT = ws + WS_WOUT + (size_t)l * D * D; K = D; N = D; f8 = true; }
;     else if ((r -= IT_OUT) < NE * IT_W1) { const int e = r / IT_W1; r %= IT_W1; W = inp(KA, I_WEXPIN) + ((size_t)l * NE + e) * D * 2048; WT = ws + WS_W1 + ((size_t)l * NE + e) * 2048 * D; K = D; N = 2048; H = 1024; f8 = true; }
;     else { r -= NE * IT_W1; const int e = r / IT_W2; r %= IT_W2; W = inp(KA, I_WEXPOUT) + ((size_t)l * NE + e) * DFF * D; WT = ws + WS_W2 + ((size_t)l * NE + e) * D * DFF; K = DFF; N = D; f8 = true; }
;     const int nblk = N / 64, kb = r / nblk, nb = r % nblk, n0 = nb * 64;
;     d.W = W; d.WT = WT; d.N = N; d.Kd = Kd ? Kd : K; d.kofs = kofs; d.drow0 = (H ? imap(n0, H) : n0) - nsub; d.k0 = kb * 64; d.n0 = n0; d.f8 = f8;
.LBB0_684:
	s_xor_b64 s[34:35], s[8:9], -1
	s_add_i32 s2, s63, s95
	s_lshl_b32 s2, s2, 4
	s_or_b32 s2, s2, s100
	s_cmpk_gt_i32 s2, 0x5fff
	s_cselect_b64 s[16:17], -1, 0
	s_cmpk_lt_i32 s2, 0x6000
	s_cselect_b64 s[42:43], -1, 0
	s_and_b64 s[0:1], s[42:43], exec
	s_cselect_b32 s44, s2, 0
	s_add_i32 s1, s44, 0x680
	s_cmpk_gt_i32 s44, 0xfd7f
	s_mov_b64 s[18:19], -1
	s_cbranch_scc0 .LBB0_704
	s_mov_b64 s[8:9], -1
	s_cmpk_gt_u32 s1, 0x47f
	s_cbranch_scc0 .LBB0_701
	s_cmpk_gt_u32 s1, 0x4ff
	s_cbranch_scc0 .LBB0_698
	s_cmpk_gt_u32 s1, 0x57f
	s_mov_b64 s[2:3], -1
	s_cbranch_scc0 .LBB0_696
	s_cmp_lt_u32 s44, 0xfffff980
	s_cbranch_scc0 .LBB0_693
	s_mov_b64 s[36:37], -1
	s_cmpk_gt_u32 s1, 0x467f
	s_cbranch_scc0 .LBB0_691
	s_add_i32 s0, s44, 0xffffc000
	s_lshr_b32 s2, s0, 8
	s_load_dwordx2 s[18:19], s[6:7], 0xd0
	s_mov_b32 s3, s59
	s_and_b32 s39, s44, 0xff
	s_lshl_b64 s[2:3], s[2:3], 20
	v_readlane_b32 s28, v255, 16
	v_readlane_b32 s29, v255, 17
	s_add_u32 s2, s2, s28
	s_addc_u32 s3, s3, s29
	s_lshl_b64 s[28:29], s[2:3], 2
	s_waitcnt lgkmcnt(0)
	s_add_u32 s56, s18, s28
	s_addc_u32 s57, s19, s29
	v_readlane_b32 s0, v253, 45
	s_add_u32 s28, s0, s2
	v_readlane_b32 s0, v253, 46
	s_addc_u32 s29, s0, s3
	s_mov_b64 s[2:3], 0
